# v96 + lever 9 (loop-edge/layout): the never-taken score-shift blocks of the 14 attention tile-loop halves moved out of line, hot path falls through instead of a taken s_branch per iteration
# speedup vs baseline: 1.0182x; 1.0182x over previous
.LBB0_502:
	s_nop 0
	v_exp_f32_e32 v80, v98
	v_exp_f32_e32 v81, v99
	v_exp_f32_e32 v82, v100
	v_exp_f32_e32 v83, v101
	v_exp_f32_e32 v84, v102
	v_exp_f32_e32 v85, v103
	v_exp_f32_e32 v86, v104
	v_exp_f32_e32 v87, v105
	v_exp_f32_e32 v88, v106
	v_exp_f32_e32 v89, v107
	v_exp_f32_e32 v90, v108
	v_exp_f32_e32 v91, v109
	v_exp_f32_e32 v92, v110
	v_exp_f32_e32 v93, v111
	v_exp_f32_e32 v94, v112
	s_cbranch_execz .LBB0_506
.LBB0_507:
	v_exp_f32_e32 v79, v97
	v_exp_f32_e32 v95, v113
	v_cvt_pk_bf16_f32 v96, v64, v65
	v_cvt_pk_bf16_f32 v97, v66, v67
	v_cvt_pk_bf16_f32 v98, v68, v69
	v_cvt_pk_bf16_f32 v99, v70, v71
	v_cvt_pk_bf16_f32 v100, v72, v73
	v_cvt_pk_bf16_f32 v101, v74, v75
	v_cvt_pk_bf16_f32 v102, v76, v77
	v_cvt_pk_bf16_f32 v103, v78, v79
	v_cvt_pk_bf16_f32 v104, v80, v81
	v_cvt_pk_bf16_f32 v105, v82, v83
	v_cvt_pk_bf16_f32 v106, v84, v85
	v_cvt_pk_bf16_f32 v107, v86, v87
	v_cvt_pk_bf16_f32 v108, v88, v89
	v_cvt_pk_bf16_f32 v109, v90, v91
	v_cvt_pk_bf16_f32 v110, v92, v93
	v_cvt_pk_bf16_f32 v111, v94, v95
	v_permlane32_swap_b32_e32 v96, v98
	v_permlane32_swap_b32_e32 v97, v99
	v_permlane32_swap_b32_e32 v100, v102
	v_permlane32_swap_b32_e32 v101, v103
	v_permlane32_swap_b32_e32 v104, v106
	v_permlane32_swap_b32_e32 v105, v107
	v_permlane32_swap_b32_e32 v108, v110
	v_permlane32_swap_b32_e32 v109, v111
	s_cmp_lt_u32 s63, 30
	s_waitcnt vmcnt(0)
	s_cselect_b64 s[22:23], -1, 0
	s_cmp_gt_u32 s63, 29
	s_cselect_b64 s[2:3], -1, 0
	s_and_b64 vcc, exec, s[2:3]
	s_waitcnt vmcnt(2)
	ds_write_b128 v211, v[178:181] offset:49152
	s_waitcnt vmcnt(1)
	ds_write_b128 v213, v[182:185] offset:16384
	s_waitcnt vmcnt(0)
	ds_write_b128 v214, v[186:189] offset:16384
	s_waitcnt lgkmcnt(0)
	s_barrier
	s_cbranch_vccnz .LBB0_509
	v_add_co_u32_e32 v112, vcc, 0x64d0000, v140
	s_nop 1
	v_addc_co_u32_e32 v113, vcc, 0, v141, vcc
	v_add_co_u32_e32 v114, vcc, 0x64d0000, v138
	s_nop 1
	v_addc_co_u32_e32 v115, vcc, 0, v139, vcc
	global_load_dwordx4 v[178:181], v[112:113], off offset:1024
	global_load_dwordx4 v[182:185], v[114:115], off offset:2048
	v_add_co_u32_e32 v112, vcc, 0x64d0000, v136
	s_nop 1
	v_addc_co_u32_e32 v113, vcc, 0, v137, vcc
	global_load_dwordx4 v[186:189], v[112:113], off offset:2048

.LBB0_512:
	s_nop 2
	v_exp_f32_e32 v144, v128
	v_exp_f32_e32 v145, v129
	v_exp_f32_e32 v146, v130
	v_exp_f32_e32 v147, v131
	v_exp_f32_e32 v148, v132
	v_exp_f32_e32 v149, v133
	v_exp_f32_e32 v150, v134
	v_exp_f32_e32 v151, v135
	v_exp_f32_e32 v152, v136
	v_exp_f32_e32 v153, v137
	v_exp_f32_e32 v154, v138
	v_exp_f32_e32 v155, v139
	v_exp_f32_e32 v156, v140
	v_exp_f32_e32 v157, v141
	v_exp_f32_e32 v158, v142
	s_cbranch_execz .LBB0_516
.LBB0_517:
	v_exp_f32_e32 v111, v127
	v_exp_f32_e32 v159, v143
	v_cvt_pk_bf16_f32 v112, v96, v97
	v_cvt_pk_bf16_f32 v113, v98, v99
	v_cvt_pk_bf16_f32 v114, v100, v101
	v_cvt_pk_bf16_f32 v115, v102, v103
	v_cvt_pk_bf16_f32 v116, v104, v105
	v_cvt_pk_bf16_f32 v117, v106, v107
	v_cvt_pk_bf16_f32 v118, v108, v109
	v_cvt_pk_bf16_f32 v119, v110, v111
	v_cvt_pk_bf16_f32 v124, v144, v145
	v_cvt_pk_bf16_f32 v125, v146, v147
	v_cvt_pk_bf16_f32 v126, v148, v149
	v_cvt_pk_bf16_f32 v127, v150, v151
	v_cvt_pk_bf16_f32 v120, v152, v153
	v_cvt_pk_bf16_f32 v121, v154, v155
	v_cvt_pk_bf16_f32 v122, v156, v157
	v_cvt_pk_bf16_f32 v123, v158, v159
	v_permlane32_swap_b32_e32 v112, v114
	v_permlane32_swap_b32_e32 v113, v115
	v_permlane32_swap_b32_e32 v116, v118
	v_permlane32_swap_b32_e32 v117, v119
	v_permlane32_swap_b32_e32 v124, v126
	v_permlane32_swap_b32_e32 v125, v127
	v_permlane32_swap_b32_e32 v120, v122
	v_permlane32_swap_b32_e32 v121, v123
	s_andn2_b64 vcc, exec, s[22:23]
	s_cbranch_vccnz .LBB0_496
	s_waitcnt vmcnt(0)
	s_waitcnt vmcnt(2)
	ds_write_b128 v211, v[178:181] offset:32768
	s_waitcnt vmcnt(1)
	ds_write_b128 v213, v[182:185]
	s_waitcnt vmcnt(0)
	ds_write_b128 v214, v[186:189]
	s_branch .LBB0_496

.LBB0_526:
	s_nop 1
	v_exp_f32_e32 v80, v96
	v_exp_f32_e32 v81, v97
	v_exp_f32_e32 v82, v98
	v_exp_f32_e32 v83, v99
	v_exp_f32_e32 v84, v100
	v_exp_f32_e32 v85, v101
	v_exp_f32_e32 v86, v102
	v_exp_f32_e32 v87, v103
	v_exp_f32_e32 v88, v104
	v_exp_f32_e32 v89, v105
	v_exp_f32_e32 v90, v106
	v_exp_f32_e32 v91, v107
	v_exp_f32_e32 v92, v108
	v_exp_f32_e32 v93, v109
	v_exp_f32_e32 v94, v110
	s_cbranch_execz .LBB0_530
.LBB0_531:
	v_exp_f32_e32 v79, v127
	v_exp_f32_e32 v95, v111
	v_cvt_pk_bf16_f32 v96, v64, v65
	v_cvt_pk_bf16_f32 v97, v66, v67
	v_cvt_pk_bf16_f32 v98, v68, v69
	v_cvt_pk_bf16_f32 v99, v70, v71
	v_cvt_pk_bf16_f32 v100, v72, v73
	v_cvt_pk_bf16_f32 v101, v74, v75
	v_cvt_pk_bf16_f32 v102, v76, v77
	v_cvt_pk_bf16_f32 v103, v78, v79
	v_cvt_pk_bf16_f32 v104, v80, v81
	v_cvt_pk_bf16_f32 v105, v82, v83
	v_cvt_pk_bf16_f32 v106, v84, v85
	v_cvt_pk_bf16_f32 v107, v86, v87
	v_cvt_pk_bf16_f32 v108, v88, v89
	v_cvt_pk_bf16_f32 v109, v90, v91
	v_cvt_pk_bf16_f32 v110, v92, v93
	v_cvt_pk_bf16_f32 v111, v94, v95
	v_permlane32_swap_b32_e32 v96, v98
	v_permlane32_swap_b32_e32 v97, v99
	v_permlane32_swap_b32_e32 v100, v102
	v_permlane32_swap_b32_e32 v101, v103
	v_permlane32_swap_b32_e32 v104, v106
	v_permlane32_swap_b32_e32 v105, v107
	v_permlane32_swap_b32_e32 v108, v110
	v_permlane32_swap_b32_e32 v109, v111
	s_barrier
	ds_read_b64_tr_b16 v[112:113], v212 offset:0
	ds_read_b64_tr_b16 v[114:115], v212 offset:0x800
	ds_read_b64_tr_b16 v[116:117], v212 offset:0x1000
	ds_read_b64_tr_b16 v[118:119], v212 offset:0x1800
	ds_read_b64_tr_b16 v[120:121], v212 offset:0x2000
	ds_read_b64_tr_b16 v[122:123], v212 offset:0x2800
	ds_read_b64_tr_b16 v[124:125], v212 offset:0x3000
	ds_read_b64_tr_b16 v[126:127], v212 offset:0x3800
	s_waitcnt lgkmcnt(0)
	s_nop 0
	v_mfma_f32_32x32x16_bf16 v[0:15], v[96:99], v[112:115], v[0:15]
	ds_read_b64_tr_b16 v[112:113], v212 offset:0x200
	ds_read_b64_tr_b16 v[114:115], v212 offset:0xa00
	v_mfma_f32_32x32x16_bf16 v[0:15], v[100:103], v[116:119], v[0:15]
	ds_read_b64_tr_b16 v[116:117], v212 offset:0x1200
	ds_read_b64_tr_b16 v[118:119], v212 offset:0x1a00
	v_mfma_f32_32x32x16_bf16 v[0:15], v[104:107], v[120:123], v[0:15]
	ds_read_b64_tr_b16 v[120:121], v212 offset:0x2200
	ds_read_b64_tr_b16 v[122:123], v212 offset:0x2a00
	v_mfma_f32_32x32x16_bf16 v[0:15], v[108:111], v[124:127], v[0:15]
	ds_read_b64_tr_b16 v[124:125], v212 offset:0x3200
	ds_read_b64_tr_b16 v[126:127], v212 offset:0x3a00
	s_waitcnt lgkmcnt(0)
	v_mfma_f32_32x32x16_bf16 v[16:31], v[96:99], v[112:115], v[16:31]
	ds_read_b64_tr_b16 v[112:113], v212 offset:0x400
	ds_read_b64_tr_b16 v[114:115], v212 offset:0xc00
	v_mfma_f32_32x32x16_bf16 v[16:31], v[100:103], v[116:119], v[16:31]
	ds_read_b64_tr_b16 v[116:117], v212 offset:0x1400
	ds_read_b64_tr_b16 v[118:119], v212 offset:0x1c00
	v_mfma_f32_32x32x16_bf16 v[16:31], v[104:107], v[120:123], v[16:31]
	ds_read_b64_tr_b16 v[120:121], v212 offset:0x2400
	ds_read_b64_tr_b16 v[122:123], v212 offset:0x2c00
	v_mfma_f32_32x32x16_bf16 v[16:31], v[108:111], v[124:127], v[16:31]
	ds_read_b64_tr_b16 v[124:125], v212 offset:0x3400
	ds_read_b64_tr_b16 v[126:127], v212 offset:0x3c00
	s_waitcnt lgkmcnt(0)
	v_mfma_f32_32x32x16_bf16 v[32:47], v[96:99], v[112:115], v[32:47]
	ds_read_b64_tr_b16 v[112:113], v212 offset:0x600
	ds_read_b64_tr_b16 v[114:115], v212 offset:0xe00
	v_mfma_f32_32x32x16_bf16 v[32:47], v[100:103], v[116:119], v[32:47]
	ds_read_b64_tr_b16 v[116:117], v212 offset:0x1600
	ds_read_b64_tr_b16 v[118:119], v212 offset:0x1e00
	v_mfma_f32_32x32x16_bf16 v[32:47], v[104:107], v[120:123], v[32:47]
	ds_read_b64_tr_b16 v[120:121], v212 offset:0x2600
	ds_read_b64_tr_b16 v[122:123], v212 offset:0x2e00
	v_mfma_f32_32x32x16_bf16 v[32:47], v[108:111], v[124:127], v[32:47]
	ds_read_b64_tr_b16 v[124:125], v212 offset:0x3600
	ds_read_b64_tr_b16 v[126:127], v212 offset:0x3e00
	s_waitcnt lgkmcnt(0)
	v_mfma_f32_32x32x16_bf16 v[48:63], v[96:99], v[112:115], v[48:63]
	s_cmp_lt_u32 s63, 30
	s_waitcnt vmcnt(0)
	s_cselect_b64 s[22:23], -1, 0
	s_cmp_gt_u32 s63, 29
	s_cselect_b64 s[2:3], -1, 0
	s_and_b64 vcc, exec, s[2:3]
	s_waitcnt vmcnt(2)
	ds_write_b128 v211, v[146:149] offset:49152
	s_waitcnt vmcnt(1)
	ds_write_b128 v213, v[150:153] offset:16384
	s_waitcnt vmcnt(0)
	ds_write_b128 v214, v[154:157] offset:16384
	v_mfma_f32_32x32x16_bf16 v[48:63], v[100:103], v[116:119], v[48:63]
	s_waitcnt lgkmcnt(0)
	s_barrier
	v_mfma_f32_32x32x16_bf16 v[48:63], v[104:107], v[120:123], v[48:63]
	v_mfma_f32_32x32x16_bf16 v[48:63], v[108:111], v[124:127], v[48:63]
	s_cbranch_vccnz .LBB0_533
	v_add_co_u32_e32 v96, vcc, 0x64d0000, v132
	s_nop 1
	v_addc_co_u32_e32 v97, vcc, 0, v133, vcc
	v_add_co_u32_e32 v98, vcc, 0x64d0000, v130
	s_nop 1
	v_addc_co_u32_e32 v99, vcc, 0, v131, vcc
	global_load_dwordx4 v[146:149], v[96:97], off offset:1024
	global_load_dwordx4 v[150:153], v[98:99], off offset:2048
	v_add_co_u32_e32 v96, vcc, 0x64d0000, v128
	s_nop 1
	v_addc_co_u32_e32 v97, vcc, 0, v129, vcc
	global_load_dwordx4 v[154:157], v[96:97], off offset:2048

.LBB0_536:
	s_nop 3
	v_exp_f32_e32 v112, v130
	v_exp_f32_e32 v113, v131
	v_exp_f32_e32 v114, v132
	v_exp_f32_e32 v115, v133
	v_exp_f32_e32 v116, v134
	v_exp_f32_e32 v117, v135
	v_exp_f32_e32 v118, v136
	v_exp_f32_e32 v119, v137
	v_exp_f32_e32 v120, v138
	v_exp_f32_e32 v121, v139
	v_exp_f32_e32 v122, v140
	v_exp_f32_e32 v123, v141
	v_exp_f32_e32 v124, v142
	v_exp_f32_e32 v125, v143
	v_exp_f32_e32 v126, v144
	s_cbranch_execz .LBB0_540
.LBB0_541:
	v_exp_f32_e32 v111, v129
	s_nop 0
	v_exp_f32_e32 v127, v145
	v_cvt_pk_bf16_f32 v128, v96, v97
	v_cvt_pk_bf16_f32 v129, v98, v99
	v_cvt_pk_bf16_f32 v130, v100, v101
	v_cvt_pk_bf16_f32 v131, v102, v103
	v_cvt_pk_bf16_f32 v132, v104, v105
	v_cvt_pk_bf16_f32 v133, v106, v107
	v_cvt_pk_bf16_f32 v134, v108, v109
	v_cvt_pk_bf16_f32 v135, v110, v111
	v_cvt_pk_bf16_f32 v136, v112, v113
	v_cvt_pk_bf16_f32 v137, v114, v115
	v_cvt_pk_bf16_f32 v138, v116, v117
	v_cvt_pk_bf16_f32 v139, v118, v119
	v_cvt_pk_bf16_f32 v140, v120, v121
	v_cvt_pk_bf16_f32 v141, v122, v123
	v_cvt_pk_bf16_f32 v142, v124, v125
	v_cvt_pk_bf16_f32 v143, v126, v127
	v_permlane32_swap_b32_e32 v128, v130
	v_permlane32_swap_b32_e32 v129, v131
	v_permlane32_swap_b32_e32 v132, v134
	v_permlane32_swap_b32_e32 v133, v135
	v_permlane32_swap_b32_e32 v136, v138
	v_permlane32_swap_b32_e32 v137, v139
	v_permlane32_swap_b32_e32 v140, v142
	v_permlane32_swap_b32_e32 v141, v143
	s_barrier
	ds_read_b64_tr_b16 v[178:179], v158 offset:0
	ds_read_b64_tr_b16 v[180:181], v158 offset:0x800
	ds_read_b64_tr_b16 v[182:183], v158 offset:0x1000
	ds_read_b64_tr_b16 v[184:185], v158 offset:0x1800
	ds_read_b64_tr_b16 v[186:187], v158 offset:0x2000
	ds_read_b64_tr_b16 v[188:189], v158 offset:0x2800
	ds_read_b64_tr_b16 v[196:197], v158 offset:0x3000
	ds_read_b64_tr_b16 v[198:199], v158 offset:0x3800
	s_waitcnt lgkmcnt(0)
	s_nop 0
	v_mfma_f32_32x32x16_bf16 v[0:15], v[128:131], v[178:181], v[0:15]
	ds_read_b64_tr_b16 v[178:179], v158 offset:0x200
	ds_read_b64_tr_b16 v[180:181], v158 offset:0xa00
	v_mfma_f32_32x32x16_bf16 v[0:15], v[132:135], v[182:185], v[0:15]
	ds_read_b64_tr_b16 v[182:183], v158 offset:0x1200
	ds_read_b64_tr_b16 v[184:185], v158 offset:0x1a00
	v_mfma_f32_32x32x16_bf16 v[0:15], v[136:139], v[186:189], v[0:15]
	ds_read_b64_tr_b16 v[186:187], v158 offset:0x2200
	ds_read_b64_tr_b16 v[188:189], v158 offset:0x2a00
	v_mfma_f32_32x32x16_bf16 v[0:15], v[140:143], v[196:199], v[0:15]
	ds_read_b64_tr_b16 v[196:197], v158 offset:0x3200
	ds_read_b64_tr_b16 v[198:199], v158 offset:0x3a00
	s_waitcnt lgkmcnt(0)
	v_mfma_f32_32x32x16_bf16 v[16:31], v[128:131], v[178:181], v[16:31]
	ds_read_b64_tr_b16 v[178:179], v158 offset:0x400
	ds_read_b64_tr_b16 v[180:181], v158 offset:0xc00
	v_mfma_f32_32x32x16_bf16 v[16:31], v[132:135], v[182:185], v[16:31]
	ds_read_b64_tr_b16 v[182:183], v158 offset:0x1400
	ds_read_b64_tr_b16 v[184:185], v158 offset:0x1c00
	v_mfma_f32_32x32x16_bf16 v[16:31], v[136:139], v[186:189], v[16:31]
	ds_read_b64_tr_b16 v[186:187], v158 offset:0x2400
	ds_read_b64_tr_b16 v[188:189], v158 offset:0x2c00
	v_mfma_f32_32x32x16_bf16 v[16:31], v[140:143], v[196:199], v[16:31]
	ds_read_b64_tr_b16 v[196:197], v158 offset:0x3400
	ds_read_b64_tr_b16 v[198:199], v158 offset:0x3c00
	s_waitcnt lgkmcnt(0)
	v_mfma_f32_32x32x16_bf16 v[32:47], v[128:131], v[178:181], v[32:47]
	ds_read_b64_tr_b16 v[178:179], v158 offset:0x600
	ds_read_b64_tr_b16 v[180:181], v158 offset:0xe00
	v_mfma_f32_32x32x16_bf16 v[32:47], v[132:135], v[182:185], v[32:47]
	ds_read_b64_tr_b16 v[182:183], v158 offset:0x1600
	ds_read_b64_tr_b16 v[184:185], v158 offset:0x1e00
	v_mfma_f32_32x32x16_bf16 v[32:47], v[136:139], v[186:189], v[32:47]
	ds_read_b64_tr_b16 v[186:187], v158 offset:0x2600
	ds_read_b64_tr_b16 v[188:189], v158 offset:0x2e00
	v_mfma_f32_32x32x16_bf16 v[32:47], v[140:143], v[196:199], v[32:47]
	ds_read_b64_tr_b16 v[196:197], v158 offset:0x3600
	ds_read_b64_tr_b16 v[198:199], v158 offset:0x3e00
	s_waitcnt lgkmcnt(0)
	v_mfma_f32_32x32x16_bf16 v[48:63], v[128:131], v[178:181], v[48:63]
	s_andn2_b64 vcc, exec, s[22:23]
	v_mfma_f32_32x32x16_bf16 v[48:63], v[132:135], v[182:185], v[48:63]
	v_mfma_f32_32x32x16_bf16 v[48:63], v[136:139], v[186:189], v[48:63]
	v_mfma_f32_32x32x16_bf16 v[48:63], v[140:143], v[196:199], v[48:63]
	s_cbranch_vccnz .LBB0_522
	s_waitcnt vmcnt(0)
	s_waitcnt vmcnt(2)
	ds_write_b128 v211, v[146:149] offset:32768
	s_waitcnt vmcnt(1)
	ds_write_b128 v213, v[150:153]
	s_waitcnt vmcnt(0)
	ds_write_b128 v214, v[154:157]
	s_branch .LBB0_522

.LBB0_553:
	s_nop 0
	v_exp_f32_e32 v80, v98
	v_exp_f32_e32 v81, v99
	v_exp_f32_e32 v82, v100
	v_exp_f32_e32 v83, v101
	v_exp_f32_e32 v84, v102
	v_exp_f32_e32 v85, v103
	v_exp_f32_e32 v86, v104
	v_exp_f32_e32 v87, v105
	v_exp_f32_e32 v88, v106
	v_exp_f32_e32 v89, v107
	v_exp_f32_e32 v90, v108
	v_exp_f32_e32 v91, v109
	v_exp_f32_e32 v92, v110
	v_exp_f32_e32 v93, v111
	v_exp_f32_e32 v94, v112
	s_cbranch_execz .LBB0_557
.LBB0_558:
	v_exp_f32_e32 v79, v97
	v_exp_f32_e32 v95, v113
	v_cvt_pk_bf16_f32 v96, v64, v65
	v_cvt_pk_bf16_f32 v97, v66, v67
	v_cvt_pk_bf16_f32 v98, v68, v69
	v_cvt_pk_bf16_f32 v99, v70, v71
	v_cvt_pk_bf16_f32 v100, v72, v73
	v_cvt_pk_bf16_f32 v101, v74, v75
	v_cvt_pk_bf16_f32 v102, v76, v77
	v_cvt_pk_bf16_f32 v103, v78, v79
	v_cvt_pk_bf16_f32 v104, v80, v81
	v_cvt_pk_bf16_f32 v105, v82, v83
	v_cvt_pk_bf16_f32 v106, v84, v85
	v_cvt_pk_bf16_f32 v107, v86, v87
	v_cvt_pk_bf16_f32 v108, v88, v89
	v_cvt_pk_bf16_f32 v109, v90, v91
	v_cvt_pk_bf16_f32 v110, v92, v93
	v_cvt_pk_bf16_f32 v111, v94, v95
	v_permlane32_swap_b32_e32 v96, v98
	v_permlane32_swap_b32_e32 v97, v99
	v_permlane32_swap_b32_e32 v100, v102
	v_permlane32_swap_b32_e32 v101, v103
	v_permlane32_swap_b32_e32 v104, v106
	v_permlane32_swap_b32_e32 v105, v107
	v_permlane32_swap_b32_e32 v108, v110
	v_permlane32_swap_b32_e32 v109, v111
	s_cmp_lt_u32 s10, 30
	s_waitcnt vmcnt(0)
	s_cselect_b64 s[22:23], -1, 0
	s_cmp_gt_u32 s10, 29
	s_cselect_b64 s[2:3], -1, 0
	s_and_b64 vcc, exec, s[2:3]
	s_waitcnt vmcnt(2)
	ds_write_b128 v211, v[178:181] offset:49152
	s_waitcnt vmcnt(1)
	ds_write_b128 v213, v[182:185] offset:16384
	s_waitcnt vmcnt(0)
	ds_write_b128 v214, v[186:189] offset:16384
	s_waitcnt lgkmcnt(0)
	s_barrier
	s_cbranch_vccnz .LBB0_560
	v_add_co_u32_e32 v112, vcc, 0x64d0000, v140
	s_nop 1
	v_addc_co_u32_e32 v113, vcc, 0, v141, vcc
	v_add_co_u32_e32 v114, vcc, 0x64d0000, v138
	s_nop 1
	v_addc_co_u32_e32 v115, vcc, 0, v139, vcc
	global_load_dwordx4 v[178:181], v[112:113], off offset:1152
	global_load_dwordx4 v[182:185], v[114:115], off offset:2048
	v_add_co_u32_e32 v112, vcc, 0x64d0000, v136
	s_nop 1
	v_addc_co_u32_e32 v113, vcc, 0, v137, vcc
	global_load_dwordx4 v[186:189], v[112:113], off offset:2048

.LBB0_563:
	s_nop 2
	v_exp_f32_e32 v144, v128
	v_exp_f32_e32 v145, v129
	v_exp_f32_e32 v146, v130
	v_exp_f32_e32 v147, v131
	v_exp_f32_e32 v148, v132
	v_exp_f32_e32 v149, v133
	v_exp_f32_e32 v150, v134
	v_exp_f32_e32 v151, v135
	v_exp_f32_e32 v152, v136
	v_exp_f32_e32 v153, v137
	v_exp_f32_e32 v154, v138
	v_exp_f32_e32 v155, v139
	v_exp_f32_e32 v156, v140
	v_exp_f32_e32 v157, v141
	v_exp_f32_e32 v158, v142
	s_cbranch_execz .LBB0_567
.LBB0_568:
	v_exp_f32_e32 v111, v127
	v_exp_f32_e32 v159, v143
	v_cvt_pk_bf16_f32 v112, v96, v97
	v_cvt_pk_bf16_f32 v113, v98, v99
	v_cvt_pk_bf16_f32 v114, v100, v101
	v_cvt_pk_bf16_f32 v115, v102, v103
	v_cvt_pk_bf16_f32 v116, v104, v105
	v_cvt_pk_bf16_f32 v117, v106, v107
	v_cvt_pk_bf16_f32 v118, v108, v109
	v_cvt_pk_bf16_f32 v119, v110, v111
	v_cvt_pk_bf16_f32 v124, v144, v145
	v_cvt_pk_bf16_f32 v125, v146, v147
	v_cvt_pk_bf16_f32 v126, v148, v149
	v_cvt_pk_bf16_f32 v127, v150, v151
	v_cvt_pk_bf16_f32 v120, v152, v153
	v_cvt_pk_bf16_f32 v121, v154, v155
	v_cvt_pk_bf16_f32 v122, v156, v157
	v_cvt_pk_bf16_f32 v123, v158, v159
	v_permlane32_swap_b32_e32 v112, v114
	v_permlane32_swap_b32_e32 v113, v115
	v_permlane32_swap_b32_e32 v116, v118
	v_permlane32_swap_b32_e32 v117, v119
	v_permlane32_swap_b32_e32 v124, v126
	v_permlane32_swap_b32_e32 v125, v127
	v_permlane32_swap_b32_e32 v120, v122
	v_permlane32_swap_b32_e32 v121, v123
	s_andn2_b64 vcc, exec, s[22:23]
	s_cbranch_vccnz .LBB0_547
	s_waitcnt vmcnt(0)
	s_waitcnt vmcnt(2)
	ds_write_b128 v211, v[178:181] offset:32768
	s_waitcnt vmcnt(1)
	ds_write_b128 v213, v[182:185]
	s_waitcnt vmcnt(0)
	ds_write_b128 v214, v[186:189]
	s_branch .LBB0_547

.LBB0_577:
	s_nop 1
	v_exp_f32_e32 v80, v96
	v_exp_f32_e32 v81, v97
	v_exp_f32_e32 v82, v98
	v_exp_f32_e32 v83, v99
	v_exp_f32_e32 v84, v100
	v_exp_f32_e32 v85, v101
	v_exp_f32_e32 v86, v102
	v_exp_f32_e32 v87, v103
	v_exp_f32_e32 v88, v104
	v_exp_f32_e32 v89, v105
	v_exp_f32_e32 v90, v106
	v_exp_f32_e32 v91, v107
	v_exp_f32_e32 v92, v108
	v_exp_f32_e32 v93, v109
	v_exp_f32_e32 v94, v110
	s_cbranch_execz .LBB0_581
.LBB0_582:
	v_exp_f32_e32 v79, v127
	v_exp_f32_e32 v95, v111
	v_cvt_pk_bf16_f32 v96, v64, v65
	v_cvt_pk_bf16_f32 v97, v66, v67
	v_cvt_pk_bf16_f32 v98, v68, v69
	v_cvt_pk_bf16_f32 v99, v70, v71
	v_cvt_pk_bf16_f32 v100, v72, v73
	v_cvt_pk_bf16_f32 v101, v74, v75
	v_cvt_pk_bf16_f32 v102, v76, v77
	v_cvt_pk_bf16_f32 v103, v78, v79
	v_cvt_pk_bf16_f32 v104, v80, v81
	v_cvt_pk_bf16_f32 v105, v82, v83
	v_cvt_pk_bf16_f32 v106, v84, v85
	v_cvt_pk_bf16_f32 v107, v86, v87
	v_cvt_pk_bf16_f32 v108, v88, v89
	v_cvt_pk_bf16_f32 v109, v90, v91
	v_cvt_pk_bf16_f32 v110, v92, v93
	v_cvt_pk_bf16_f32 v111, v94, v95
	v_permlane32_swap_b32_e32 v96, v98
	v_permlane32_swap_b32_e32 v97, v99
	v_permlane32_swap_b32_e32 v100, v102
	v_permlane32_swap_b32_e32 v101, v103
	v_permlane32_swap_b32_e32 v104, v106
	v_permlane32_swap_b32_e32 v105, v107
	v_permlane32_swap_b32_e32 v108, v110
	v_permlane32_swap_b32_e32 v109, v111
	s_barrier
	ds_read_b64_tr_b16 v[112:113], v212 offset:0
	ds_read_b64_tr_b16 v[114:115], v212 offset:0x800
	ds_read_b64_tr_b16 v[116:117], v212 offset:0x1000
	ds_read_b64_tr_b16 v[118:119], v212 offset:0x1800
	ds_read_b64_tr_b16 v[120:121], v212 offset:0x2000
	ds_read_b64_tr_b16 v[122:123], v212 offset:0x2800
	ds_read_b64_tr_b16 v[124:125], v212 offset:0x3000
	ds_read_b64_tr_b16 v[126:127], v212 offset:0x3800
	s_waitcnt lgkmcnt(0)
	s_nop 0
	v_mfma_f32_32x32x16_bf16 v[0:15], v[96:99], v[112:115], v[0:15]
	ds_read_b64_tr_b16 v[112:113], v212 offset:0x200
	ds_read_b64_tr_b16 v[114:115], v212 offset:0xa00
	v_mfma_f32_32x32x16_bf16 v[0:15], v[100:103], v[116:119], v[0:15]
	ds_read_b64_tr_b16 v[116:117], v212 offset:0x1200
	ds_read_b64_tr_b16 v[118:119], v212 offset:0x1a00
	v_mfma_f32_32x32x16_bf16 v[0:15], v[104:107], v[120:123], v[0:15]
	ds_read_b64_tr_b16 v[120:121], v212 offset:0x2200
	ds_read_b64_tr_b16 v[122:123], v212 offset:0x2a00
	v_mfma_f32_32x32x16_bf16 v[0:15], v[108:111], v[124:127], v[0:15]
	ds_read_b64_tr_b16 v[124:125], v212 offset:0x3200
	ds_read_b64_tr_b16 v[126:127], v212 offset:0x3a00
	s_waitcnt lgkmcnt(0)
	v_mfma_f32_32x32x16_bf16 v[16:31], v[96:99], v[112:115], v[16:31]
	ds_read_b64_tr_b16 v[112:113], v212 offset:0x400
	ds_read_b64_tr_b16 v[114:115], v212 offset:0xc00
	v_mfma_f32_32x32x16_bf16 v[16:31], v[100:103], v[116:119], v[16:31]
	ds_read_b64_tr_b16 v[116:117], v212 offset:0x1400
	ds_read_b64_tr_b16 v[118:119], v212 offset:0x1c00
	v_mfma_f32_32x32x16_bf16 v[16:31], v[104:107], v[120:123], v[16:31]
	ds_read_b64_tr_b16 v[120:121], v212 offset:0x2400
	ds_read_b64_tr_b16 v[122:123], v212 offset:0x2c00
	v_mfma_f32_32x32x16_bf16 v[16:31], v[108:111], v[124:127], v[16:31]
	ds_read_b64_tr_b16 v[124:125], v212 offset:0x3400
	ds_read_b64_tr_b16 v[126:127], v212 offset:0x3c00
	s_waitcnt lgkmcnt(0)
	v_mfma_f32_32x32x16_bf16 v[32:47], v[96:99], v[112:115], v[32:47]
	ds_read_b64_tr_b16 v[112:113], v212 offset:0x600
	ds_read_b64_tr_b16 v[114:115], v212 offset:0xe00
	v_mfma_f32_32x32x16_bf16 v[32:47], v[100:103], v[116:119], v[32:47]
	ds_read_b64_tr_b16 v[116:117], v212 offset:0x1600
	ds_read_b64_tr_b16 v[118:119], v212 offset:0x1e00
	v_mfma_f32_32x32x16_bf16 v[32:47], v[104:107], v[120:123], v[32:47]
	ds_read_b64_tr_b16 v[120:121], v212 offset:0x2600
	ds_read_b64_tr_b16 v[122:123], v212 offset:0x2e00
	v_mfma_f32_32x32x16_bf16 v[32:47], v[108:111], v[124:127], v[32:47]
	ds_read_b64_tr_b16 v[124:125], v212 offset:0x3600
	ds_read_b64_tr_b16 v[126:127], v212 offset:0x3e00
	s_waitcnt lgkmcnt(0)
	v_mfma_f32_32x32x16_bf16 v[48:63], v[96:99], v[112:115], v[48:63]
	s_cmp_lt_u32 s6, 30
	s_waitcnt vmcnt(0)
	s_cselect_b64 s[22:23], -1, 0
	s_cmp_gt_u32 s6, 29
	s_cselect_b64 s[2:3], -1, 0
	s_and_b64 vcc, exec, s[2:3]
	s_waitcnt vmcnt(2)
	ds_write_b128 v211, v[146:149] offset:49152
	s_waitcnt vmcnt(1)
	ds_write_b128 v213, v[150:153] offset:16384
	s_waitcnt vmcnt(0)
	ds_write_b128 v214, v[154:157] offset:16384
	v_mfma_f32_32x32x16_bf16 v[48:63], v[100:103], v[116:119], v[48:63]
	s_waitcnt lgkmcnt(0)
	s_barrier
	v_mfma_f32_32x32x16_bf16 v[48:63], v[104:107], v[120:123], v[48:63]
	v_mfma_f32_32x32x16_bf16 v[48:63], v[108:111], v[124:127], v[48:63]
	s_cbranch_vccnz .LBB0_584
	v_add_co_u32_e32 v96, vcc, 0x64d0000, v132
	s_nop 1
	v_addc_co_u32_e32 v97, vcc, 0, v133, vcc
	v_add_co_u32_e32 v98, vcc, 0x64d0000, v130
	s_nop 1
	v_addc_co_u32_e32 v99, vcc, 0, v131, vcc
	global_load_dwordx4 v[146:149], v[96:97], off offset:1152
	global_load_dwordx4 v[150:153], v[98:99], off offset:2048
	v_add_co_u32_e32 v96, vcc, 0x64d0000, v128
	s_nop 1
	v_addc_co_u32_e32 v97, vcc, 0, v129, vcc
	global_load_dwordx4 v[154:157], v[96:97], off offset:2048

.LBB0_587:
	s_nop 3
	v_exp_f32_e32 v112, v130
	v_exp_f32_e32 v113, v131
	v_exp_f32_e32 v114, v132
	v_exp_f32_e32 v115, v133
	v_exp_f32_e32 v116, v134
	v_exp_f32_e32 v117, v135
	v_exp_f32_e32 v118, v136
	v_exp_f32_e32 v119, v137
	v_exp_f32_e32 v120, v138
	v_exp_f32_e32 v121, v139
	v_exp_f32_e32 v122, v140
	v_exp_f32_e32 v123, v141
	v_exp_f32_e32 v124, v142
	v_exp_f32_e32 v125, v143
	v_exp_f32_e32 v126, v144
	s_cbranch_execz .LBB0_591
.LBB0_592:
	v_exp_f32_e32 v111, v129
	s_nop 0
	v_exp_f32_e32 v127, v145
	v_cvt_pk_bf16_f32 v128, v96, v97
	v_cvt_pk_bf16_f32 v129, v98, v99
	v_cvt_pk_bf16_f32 v130, v100, v101
	v_cvt_pk_bf16_f32 v131, v102, v103
	v_cvt_pk_bf16_f32 v132, v104, v105
	v_cvt_pk_bf16_f32 v133, v106, v107
	v_cvt_pk_bf16_f32 v134, v108, v109
	v_cvt_pk_bf16_f32 v135, v110, v111
	v_cvt_pk_bf16_f32 v136, v112, v113
	v_cvt_pk_bf16_f32 v137, v114, v115
	v_cvt_pk_bf16_f32 v138, v116, v117
	v_cvt_pk_bf16_f32 v139, v118, v119
	v_cvt_pk_bf16_f32 v140, v120, v121
	v_cvt_pk_bf16_f32 v141, v122, v123
	v_cvt_pk_bf16_f32 v142, v124, v125
	v_cvt_pk_bf16_f32 v143, v126, v127
	v_permlane32_swap_b32_e32 v128, v130
	v_permlane32_swap_b32_e32 v129, v131
	v_permlane32_swap_b32_e32 v132, v134
	v_permlane32_swap_b32_e32 v133, v135
	v_permlane32_swap_b32_e32 v136, v138
	v_permlane32_swap_b32_e32 v137, v139
	v_permlane32_swap_b32_e32 v140, v142
	v_permlane32_swap_b32_e32 v141, v143
	s_barrier
	ds_read_b64_tr_b16 v[178:179], v158 offset:0
	ds_read_b64_tr_b16 v[180:181], v158 offset:0x800
	ds_read_b64_tr_b16 v[182:183], v158 offset:0x1000
	ds_read_b64_tr_b16 v[184:185], v158 offset:0x1800
	ds_read_b64_tr_b16 v[186:187], v158 offset:0x2000
	ds_read_b64_tr_b16 v[188:189], v158 offset:0x2800
	ds_read_b64_tr_b16 v[196:197], v158 offset:0x3000
	ds_read_b64_tr_b16 v[198:199], v158 offset:0x3800
	s_waitcnt lgkmcnt(0)
	s_nop 0
	v_mfma_f32_32x32x16_bf16 v[0:15], v[128:131], v[178:181], v[0:15]
	ds_read_b64_tr_b16 v[178:179], v158 offset:0x200
	ds_read_b64_tr_b16 v[180:181], v158 offset:0xa00
	v_mfma_f32_32x32x16_bf16 v[0:15], v[132:135], v[182:185], v[0:15]
	ds_read_b64_tr_b16 v[182:183], v158 offset:0x1200
	ds_read_b64_tr_b16 v[184:185], v158 offset:0x1a00
	v_mfma_f32_32x32x16_bf16 v[0:15], v[136:139], v[186:189], v[0:15]
	ds_read_b64_tr_b16 v[186:187], v158 offset:0x2200
	ds_read_b64_tr_b16 v[188:189], v158 offset:0x2a00
	v_mfma_f32_32x32x16_bf16 v[0:15], v[140:143], v[196:199], v[0:15]
	ds_read_b64_tr_b16 v[196:197], v158 offset:0x3200
	ds_read_b64_tr_b16 v[198:199], v158 offset:0x3a00
	s_waitcnt lgkmcnt(0)
	v_mfma_f32_32x32x16_bf16 v[16:31], v[128:131], v[178:181], v[16:31]
	ds_read_b64_tr_b16 v[178:179], v158 offset:0x400
	ds_read_b64_tr_b16 v[180:181], v158 offset:0xc00
	v_mfma_f32_32x32x16_bf16 v[16:31], v[132:135], v[182:185], v[16:31]
	ds_read_b64_tr_b16 v[182:183], v158 offset:0x1400
	ds_read_b64_tr_b16 v[184:185], v158 offset:0x1c00
	v_mfma_f32_32x32x16_bf16 v[16:31], v[136:139], v[186:189], v[16:31]
	ds_read_b64_tr_b16 v[186:187], v158 offset:0x2400
	ds_read_b64_tr_b16 v[188:189], v158 offset:0x2c00
	v_mfma_f32_32x32x16_bf16 v[16:31], v[140:143], v[196:199], v[16:31]
	ds_read_b64_tr_b16 v[196:197], v158 offset:0x3400
	ds_read_b64_tr_b16 v[198:199], v158 offset:0x3c00
	s_waitcnt lgkmcnt(0)
	v_mfma_f32_32x32x16_bf16 v[32:47], v[128:131], v[178:181], v[32:47]
	ds_read_b64_tr_b16 v[178:179], v158 offset:0x600
	ds_read_b64_tr_b16 v[180:181], v158 offset:0xe00
	v_mfma_f32_32x32x16_bf16 v[32:47], v[132:135], v[182:185], v[32:47]
	ds_read_b64_tr_b16 v[182:183], v158 offset:0x1600
	ds_read_b64_tr_b16 v[184:185], v158 offset:0x1e00
	v_mfma_f32_32x32x16_bf16 v[32:47], v[136:139], v[186:189], v[32:47]
	ds_read_b64_tr_b16 v[186:187], v158 offset:0x2600
	ds_read_b64_tr_b16 v[188:189], v158 offset:0x2e00
	v_mfma_f32_32x32x16_bf16 v[32:47], v[140:143], v[196:199], v[32:47]
	ds_read_b64_tr_b16 v[196:197], v158 offset:0x3600
	ds_read_b64_tr_b16 v[198:199], v158 offset:0x3e00
	s_waitcnt lgkmcnt(0)
	v_mfma_f32_32x32x16_bf16 v[48:63], v[128:131], v[178:181], v[48:63]
	s_andn2_b64 vcc, exec, s[22:23]
	v_mfma_f32_32x32x16_bf16 v[48:63], v[132:135], v[182:185], v[48:63]
	v_mfma_f32_32x32x16_bf16 v[48:63], v[136:139], v[186:189], v[48:63]
	v_mfma_f32_32x32x16_bf16 v[48:63], v[140:143], v[196:199], v[48:63]
	s_cbranch_vccnz .LBB0_573
	s_waitcnt vmcnt(0)
	s_waitcnt vmcnt(2)
	ds_write_b128 v211, v[146:149] offset:32768
	s_waitcnt vmcnt(1)
	ds_write_b128 v213, v[150:153]
	s_waitcnt vmcnt(0)
	ds_write_b128 v214, v[154:157]
	s_branch .LBB0_573
.LBB0_594:
	v_and_b32_e32 v64, 0x1c0, v205
	v_mov_b32_e32 v65, v215
	v_lshl_add_u32 v64, v64, 2, s63
	s_nop 0
	v_permlane32_swap_b32_e32 v215, v65
	v_cmp_gt_u32_e32 vcc, 32, v191
	s_and_saveexec_b64 s[2:3], vcc
	s_cbranch_execz .LBB0_493
	v_add_f32_e32 v65, v215, v65
	v_lshl_add_u32 v66, v203, 2, v64
	ds_write_b32 v66, v65
	s_branch .LBB0_493
.LBB0_503:
	s_andn2_b64 vcc, exec, s[2:3]
	s_cbranch_vccnz .LBB0_501

.LBB0_506:
	v_add_f32_e32 v79, s31, v98
	v_exp_f32_e32 v80, v79
	v_add_f32_e32 v79, s31, v99
	v_exp_f32_e32 v81, v79
	v_add_f32_e32 v79, s31, v100
	v_exp_f32_e32 v82, v79
	v_add_f32_e32 v79, s31, v101
	v_exp_f32_e32 v83, v79
	v_add_f32_e32 v79, s31, v102
	v_exp_f32_e32 v84, v79
	v_add_f32_e32 v79, s31, v103
	v_exp_f32_e32 v85, v79
	v_add_f32_e32 v79, s31, v104
	v_exp_f32_e32 v86, v79
	v_add_f32_e32 v79, s31, v105
	v_exp_f32_e32 v87, v79
	v_add_f32_e32 v79, s31, v106
	v_exp_f32_e32 v88, v79
	v_add_f32_e32 v79, s31, v107
	v_exp_f32_e32 v89, v79
	v_add_f32_e32 v79, s31, v108
	v_exp_f32_e32 v90, v79
	v_add_f32_e32 v79, s31, v109
	v_exp_f32_e32 v91, v79
	v_add_f32_e32 v79, s31, v110
	v_exp_f32_e32 v92, v79
	v_add_f32_e32 v79, s31, v111
	v_exp_f32_e32 v93, v79
	v_add_f32_e32 v79, s31, v112
	v_exp_f32_e32 v94, v79
	v_add_f32_e32 v113, s31, v113
	s_branch .LBB0_507

.LBB0_516:
	s_nop 0
	v_add_f32_e32 v111, s31, v128
	v_exp_f32_e32 v144, v111
	v_add_f32_e32 v111, s31, v129
	v_exp_f32_e32 v145, v111
	v_add_f32_e32 v111, s31, v130
	v_exp_f32_e32 v146, v111
	v_add_f32_e32 v111, s31, v131
	v_exp_f32_e32 v147, v111
	v_add_f32_e32 v111, s31, v132
	v_exp_f32_e32 v148, v111
	v_add_f32_e32 v111, s31, v133
	v_exp_f32_e32 v149, v111
	v_add_f32_e32 v111, s31, v134
	v_exp_f32_e32 v150, v111
	v_add_f32_e32 v111, s31, v135
	v_exp_f32_e32 v151, v111
	v_add_f32_e32 v111, s31, v136
	v_exp_f32_e32 v152, v111
	v_add_f32_e32 v111, s31, v137
	v_exp_f32_e32 v153, v111
	v_add_f32_e32 v111, s31, v138
	v_exp_f32_e32 v154, v111
	v_add_f32_e32 v111, s31, v139
	v_exp_f32_e32 v155, v111
	v_add_f32_e32 v111, s31, v140
	v_exp_f32_e32 v156, v111
	v_add_f32_e32 v111, s31, v141
	v_exp_f32_e32 v157, v111
	v_add_f32_e32 v111, s31, v142
	v_exp_f32_e32 v158, v111
	v_add_f32_e32 v143, s31, v143
	s_branch .LBB0_517

.LBB0_530:
	v_add_f32_e32 v79, s31, v96
	v_exp_f32_e32 v80, v79
	v_add_f32_e32 v79, s31, v97
	v_exp_f32_e32 v81, v79
	v_add_f32_e32 v79, s31, v98
	v_exp_f32_e32 v82, v79
	v_add_f32_e32 v79, s31, v99
	v_exp_f32_e32 v83, v79
	v_add_f32_e32 v79, s31, v100
	v_exp_f32_e32 v84, v79
	v_add_f32_e32 v79, s31, v101
	v_exp_f32_e32 v85, v79
	v_add_f32_e32 v79, s31, v102
	v_exp_f32_e32 v86, v79
	v_add_f32_e32 v79, s31, v103
	v_exp_f32_e32 v87, v79
	v_add_f32_e32 v79, s31, v104
	v_exp_f32_e32 v88, v79
	v_add_f32_e32 v79, s31, v105
	v_exp_f32_e32 v89, v79
	v_add_f32_e32 v79, s31, v106
	v_exp_f32_e32 v90, v79
	v_add_f32_e32 v79, s31, v107
	v_exp_f32_e32 v91, v79
	v_add_f32_e32 v79, s31, v108
	v_exp_f32_e32 v92, v79
	v_add_f32_e32 v79, s31, v109
	v_exp_f32_e32 v93, v79
	v_add_f32_e32 v79, s31, v110
	v_exp_f32_e32 v94, v79
	v_add_f32_e32 v111, s31, v111
	s_branch .LBB0_531

.LBB0_540:
	s_nop 1
	v_add_f32_e32 v111, s31, v130
	v_exp_f32_e32 v112, v111
	v_add_f32_e32 v111, s31, v131
	v_exp_f32_e32 v113, v111
	v_add_f32_e32 v111, s31, v132
	v_exp_f32_e32 v114, v111
	v_add_f32_e32 v111, s31, v133
	v_exp_f32_e32 v115, v111
	v_add_f32_e32 v111, s31, v134
	v_exp_f32_e32 v116, v111
	v_add_f32_e32 v111, s31, v135
	v_exp_f32_e32 v117, v111
	v_add_f32_e32 v111, s31, v136
	v_exp_f32_e32 v118, v111
	v_add_f32_e32 v111, s31, v137
	v_exp_f32_e32 v119, v111
	v_add_f32_e32 v111, s31, v138
	v_exp_f32_e32 v120, v111
	v_add_f32_e32 v111, s31, v139
	v_exp_f32_e32 v121, v111
	v_add_f32_e32 v111, s31, v140
	v_exp_f32_e32 v122, v111
	v_add_f32_e32 v111, s31, v141
	v_exp_f32_e32 v123, v111
	v_add_f32_e32 v111, s31, v142
	v_exp_f32_e32 v124, v111
	v_add_f32_e32 v111, s31, v143
	v_exp_f32_e32 v125, v111
	v_add_f32_e32 v111, s31, v144
	v_exp_f32_e32 v126, v111
	v_add_f32_e32 v145, s31, v145
	s_branch .LBB0_541

.LBB0_613:
	v_add_f32_e32 v111, s33, v130
	v_exp_f32_e32 v112, v111
	v_add_f32_e32 v111, s33, v131
	v_exp_f32_e32 v113, v111
	v_add_f32_e32 v111, s33, v132
	v_exp_f32_e32 v114, v111
	v_add_f32_e32 v111, s33, v133
	v_exp_f32_e32 v115, v111
	v_add_f32_e32 v111, s33, v134
	v_exp_f32_e32 v116, v111
	v_add_f32_e32 v111, s33, v135
	v_exp_f32_e32 v117, v111
	v_add_f32_e32 v111, s33, v136
	v_exp_f32_e32 v118, v111
	v_add_f32_e32 v111, s33, v137
	v_exp_f32_e32 v119, v111
	v_add_f32_e32 v111, s33, v138
	v_exp_f32_e32 v120, v111
	v_add_f32_e32 v111, s33, v139
	v_exp_f32_e32 v121, v111
	v_add_f32_e32 v111, s33, v140
	v_exp_f32_e32 v122, v111
	v_add_f32_e32 v111, s33, v141
	v_exp_f32_e32 v123, v111
	v_add_f32_e32 v111, s33, v142
	v_exp_f32_e32 v124, v111
	v_add_f32_e32 v111, s33, v143
	v_exp_f32_e32 v125, v111
	v_add_f32_e32 v111, s33, v144
	v_exp_f32_e32 v126, v111
	v_add_f32_e32 v145, s33, v145
	s_branch .LBB0_614

.LBB0_643:
	v_add_f32_e32 v111, s77, v130
	v_exp_f32_e32 v112, v111
	v_add_f32_e32 v111, s77, v131
	v_exp_f32_e32 v113, v111
	v_add_f32_e32 v111, s77, v132
	v_exp_f32_e32 v114, v111
	v_add_f32_e32 v111, s77, v133
	v_exp_f32_e32 v115, v111
	v_add_f32_e32 v111, s77, v134
	v_exp_f32_e32 v116, v111
	v_add_f32_e32 v111, s77, v135
	v_exp_f32_e32 v117, v111
	v_add_f32_e32 v111, s77, v136
	v_exp_f32_e32 v118, v111
	v_add_f32_e32 v111, s77, v137
	v_exp_f32_e32 v119, v111
	v_add_f32_e32 v111, s77, v138
	v_exp_f32_e32 v120, v111
	v_add_f32_e32 v111, s77, v139
	v_exp_f32_e32 v121, v111
	v_add_f32_e32 v111, s77, v140
	v_exp_f32_e32 v122, v111
	v_add_f32_e32 v111, s77, v141
	v_exp_f32_e32 v123, v111
	v_add_f32_e32 v111, s77, v142
	v_exp_f32_e32 v124, v111
	v_add_f32_e32 v111, s77, v143
	v_exp_f32_e32 v125, v111
	v_add_f32_e32 v111, s77, v144
	v_exp_f32_e32 v126, v111
	v_add_f32_e32 v145, s77, v145
	s_branch .LBB0_644

.LBB0_670:
	v_add_f32_e32 v79, s96, v98
	v_exp_f32_e32 v80, v79
	v_add_f32_e32 v79, s96, v99
	v_exp_f32_e32 v81, v79
	v_add_f32_e32 v79, s96, v100
	v_exp_f32_e32 v82, v79
	v_add_f32_e32 v79, s96, v101
	v_exp_f32_e32 v83, v79
	v_add_f32_e32 v79, s96, v102
	v_exp_f32_e32 v84, v79
	v_add_f32_e32 v79, s96, v103
	v_exp_f32_e32 v85, v79
	v_add_f32_e32 v79, s96, v104
	v_exp_f32_e32 v86, v79
	v_add_f32_e32 v79, s96, v105
	v_exp_f32_e32 v87, v79
	v_add_f32_e32 v79, s96, v106
	v_exp_f32_e32 v88, v79
	v_add_f32_e32 v79, s96, v107
	v_exp_f32_e32 v89, v79
	v_add_f32_e32 v79, s96, v108
	v_exp_f32_e32 v90, v79
	v_add_f32_e32 v79, s96, v109
	v_exp_f32_e32 v91, v79
	v_add_f32_e32 v79, s96, v110
	v_exp_f32_e32 v92, v79
	v_add_f32_e32 v79, s96, v111
	v_exp_f32_e32 v93, v79
	v_add_f32_e32 v79, s96, v112
	v_exp_f32_e32 v94, v79
	v_add_f32_e32 v113, s96, v113
	s_branch .LBB0_671

.LBB0_680:
	s_nop 0
	v_add_f32_e32 v111, s96, v128
	v_exp_f32_e32 v144, v111
	v_add_f32_e32 v111, s96, v129
	v_exp_f32_e32 v145, v111
	v_add_f32_e32 v111, s96, v130
	v_exp_f32_e32 v146, v111
	v_add_f32_e32 v111, s96, v131
	v_exp_f32_e32 v147, v111
	v_add_f32_e32 v111, s96, v132
	v_exp_f32_e32 v148, v111
	v_add_f32_e32 v111, s96, v133
	v_exp_f32_e32 v149, v111
	v_add_f32_e32 v111, s96, v134
	v_exp_f32_e32 v150, v111
	v_add_f32_e32 v111, s96, v135
	v_exp_f32_e32 v151, v111
	v_add_f32_e32 v111, s96, v136
	v_exp_f32_e32 v152, v111
	v_add_f32_e32 v111, s96, v137
	v_exp_f32_e32 v153, v111
	v_add_f32_e32 v111, s96, v138
	v_exp_f32_e32 v154, v111
	v_add_f32_e32 v111, s96, v139
	v_exp_f32_e32 v155, v111
	v_add_f32_e32 v111, s96, v140
	v_exp_f32_e32 v156, v111
	v_add_f32_e32 v111, s96, v141
	v_exp_f32_e32 v157, v111
	v_add_f32_e32 v111, s96, v142
	v_exp_f32_e32 v158, v111
	v_add_f32_e32 v143, s96, v143
	s_branch .LBB0_681

.LBB0_694:
	v_add_f32_e32 v79, s96, v96
	v_exp_f32_e32 v80, v79
	v_add_f32_e32 v79, s96, v97
	v_exp_f32_e32 v81, v79
	v_add_f32_e32 v79, s96, v98
	v_exp_f32_e32 v82, v79
	v_add_f32_e32 v79, s96, v99
	v_exp_f32_e32 v83, v79
	v_add_f32_e32 v79, s96, v100
	v_exp_f32_e32 v84, v79
	v_add_f32_e32 v79, s96, v101
	v_exp_f32_e32 v85, v79
	v_add_f32_e32 v79, s96, v102
	v_exp_f32_e32 v86, v79
	v_add_f32_e32 v79, s96, v103
	v_exp_f32_e32 v87, v79
	v_add_f32_e32 v79, s96, v104
	v_exp_f32_e32 v88, v79
	v_add_f32_e32 v79, s96, v105
	v_exp_f32_e32 v89, v79
	v_add_f32_e32 v79, s96, v106
	v_exp_f32_e32 v90, v79
	v_add_f32_e32 v79, s96, v107
	v_exp_f32_e32 v91, v79
	v_add_f32_e32 v79, s96, v108
	v_exp_f32_e32 v92, v79
	v_add_f32_e32 v79, s96, v109
	v_exp_f32_e32 v93, v79
	v_add_f32_e32 v79, s96, v110
	v_exp_f32_e32 v94, v79
	v_add_f32_e32 v111, s96, v111
	s_branch .LBB0_695

.LBB0_704:
	s_nop 1
	v_add_f32_e32 v111, s96, v130
	v_exp_f32_e32 v112, v111
	v_add_f32_e32 v111, s96, v131
	v_exp_f32_e32 v113, v111
	v_add_f32_e32 v111, s96, v132
	v_exp_f32_e32 v114, v111
	v_add_f32_e32 v111, s96, v133
	v_exp_f32_e32 v115, v111
	v_add_f32_e32 v111, s96, v134
	v_exp_f32_e32 v116, v111
	v_add_f32_e32 v111, s96, v135
	v_exp_f32_e32 v117, v111
	v_add_f32_e32 v111, s96, v136
	v_exp_f32_e32 v118, v111
	v_add_f32_e32 v111, s96, v137
	v_exp_f32_e32 v119, v111
	v_add_f32_e32 v111, s96, v138
	v_exp_f32_e32 v120, v111
	v_add_f32_e32 v111, s96, v139
	v_exp_f32_e32 v121, v111
	v_add_f32_e32 v111, s96, v140
	v_exp_f32_e32 v122, v111
	v_add_f32_e32 v111, s96, v141
	v_exp_f32_e32 v123, v111
	v_add_f32_e32 v111, s96, v142
	v_exp_f32_e32 v124, v111
	v_add_f32_e32 v111, s96, v143
	v_exp_f32_e32 v125, v111
	v_add_f32_e32 v111, s96, v144
	v_exp_f32_e32 v126, v111
	v_add_f32_e32 v145, s96, v145
	s_branch .LBB0_705

.LBB0_609:
	s_nop 0
	v_exp_f32_e32 v112, v130
	v_exp_f32_e32 v113, v131
	v_exp_f32_e32 v114, v132
	v_exp_f32_e32 v115, v133
	v_exp_f32_e32 v116, v134
	v_exp_f32_e32 v117, v135
	v_exp_f32_e32 v118, v136
	v_exp_f32_e32 v119, v137
	v_exp_f32_e32 v120, v138
	v_exp_f32_e32 v121, v139
	v_exp_f32_e32 v122, v140
	v_exp_f32_e32 v123, v141
	v_exp_f32_e32 v124, v142
	v_exp_f32_e32 v125, v143
	v_exp_f32_e32 v126, v144
	s_cbranch_execz .LBB0_613
.LBB0_614:
	v_exp_f32_e32 v111, v129
	v_exp_f32_e32 v127, v145
	v_cvt_pk_bf16_f32 v210, v96, v97
	v_cvt_pk_bf16_f32 v211, v98, v99
	v_cvt_pk_bf16_f32 v212, v100, v101
	v_cvt_pk_bf16_f32 v213, v102, v103
	v_cvt_pk_bf16_f32 v218, v104, v105
	v_cvt_pk_bf16_f32 v219, v106, v107
	v_cvt_pk_bf16_f32 v220, v108, v109
	v_cvt_pk_bf16_f32 v221, v110, v111
	v_cvt_pk_bf16_f32 v222, v112, v113
	v_cvt_pk_bf16_f32 v223, v114, v115
	v_cvt_pk_bf16_f32 v224, v116, v117
	v_cvt_pk_bf16_f32 v225, v118, v119
	v_cvt_pk_bf16_f32 v214, v120, v121
	v_cvt_pk_bf16_f32 v215, v122, v123
	v_cvt_pk_bf16_f32 v216, v124, v125
	v_cvt_pk_bf16_f32 v217, v126, v127
	v_permlane32_swap_b32_e32 v210, v212
	v_permlane32_swap_b32_e32 v211, v213
	v_permlane32_swap_b32_e32 v218, v220
	v_permlane32_swap_b32_e32 v219, v221
	v_permlane32_swap_b32_e32 v222, v224
	v_permlane32_swap_b32_e32 v223, v225
	v_permlane32_swap_b32_e32 v214, v216
	v_permlane32_swap_b32_e32 v215, v217
	s_and_b64 vcc, exec, s[44:45]
	s_mov_b64 s[2:3], -1
	s_cbranch_vccnz .LBB0_618
	v_exp_f32_e32 v128, v80
	v_exp_f32_e32 v129, v81
	v_exp_f32_e32 v130, v82
	v_exp_f32_e32 v131, v83
	v_exp_f32_e32 v132, v84
	v_exp_f32_e32 v133, v85
	v_exp_f32_e32 v134, v86
	v_exp_f32_e32 v135, v87
	v_exp_f32_e32 v136, v88
	v_exp_f32_e32 v137, v89
	v_exp_f32_e32 v138, v90
	v_exp_f32_e32 v139, v91
	v_exp_f32_e32 v140, v92
	v_exp_f32_e32 v141, v93
	v_exp_f32_e32 v142, v94
	s_cbranch_execz .LBB0_619

.LBB0_639:
	s_nop 0
	v_exp_f32_e32 v112, v130
	v_exp_f32_e32 v113, v131
	v_exp_f32_e32 v114, v132
	v_exp_f32_e32 v115, v133
	v_exp_f32_e32 v116, v134
	v_exp_f32_e32 v117, v135
	v_exp_f32_e32 v118, v136
	v_exp_f32_e32 v119, v137
	v_exp_f32_e32 v120, v138
	v_exp_f32_e32 v121, v139
	v_exp_f32_e32 v122, v140
	v_exp_f32_e32 v123, v141
	v_exp_f32_e32 v124, v142
	v_exp_f32_e32 v125, v143
	v_exp_f32_e32 v126, v144
	s_cbranch_execz .LBB0_643
.LBB0_644:
	v_exp_f32_e32 v111, v129
	v_exp_f32_e32 v127, v145
	v_cvt_pk_bf16_f32 v194, v96, v97
	v_cvt_pk_bf16_f32 v195, v98, v99
	v_cvt_pk_bf16_f32 v196, v100, v101
	v_cvt_pk_bf16_f32 v197, v102, v103
	v_cvt_pk_bf16_f32 v198, v104, v105
	v_cvt_pk_bf16_f32 v199, v106, v107
	v_cvt_pk_bf16_f32 v200, v108, v109
	v_cvt_pk_bf16_f32 v201, v110, v111
	v_cvt_pk_bf16_f32 v202, v112, v113
	v_cvt_pk_bf16_f32 v203, v114, v115
	v_cvt_pk_bf16_f32 v204, v116, v117
	v_cvt_pk_bf16_f32 v205, v118, v119
	v_cvt_pk_bf16_f32 v206, v120, v121
	v_cvt_pk_bf16_f32 v207, v122, v123
	v_cvt_pk_bf16_f32 v208, v124, v125
	v_cvt_pk_bf16_f32 v209, v126, v127
	v_permlane32_swap_b32_e32 v194, v196
	v_permlane32_swap_b32_e32 v195, v197
	v_permlane32_swap_b32_e32 v198, v200
	v_permlane32_swap_b32_e32 v199, v201
	v_permlane32_swap_b32_e32 v202, v204
	v_permlane32_swap_b32_e32 v203, v205
	v_permlane32_swap_b32_e32 v206, v208
	v_permlane32_swap_b32_e32 v207, v209
	s_and_b64 vcc, exec, s[44:45]
	s_mov_b64 s[2:3], -1
	s_cbranch_vccnz .LBB0_648
	v_exp_f32_e32 v128, v80
	v_exp_f32_e32 v129, v81
	v_exp_f32_e32 v130, v82
	v_exp_f32_e32 v131, v83
	v_exp_f32_e32 v132, v84
	v_exp_f32_e32 v133, v85
	v_exp_f32_e32 v134, v86
	v_exp_f32_e32 v135, v87
	v_exp_f32_e32 v136, v88
	v_exp_f32_e32 v137, v89
	v_exp_f32_e32 v138, v90
	v_exp_f32_e32 v139, v91
	v_exp_f32_e32 v140, v92
	v_exp_f32_e32 v141, v93
	v_exp_f32_e32 v142, v94
	s_cbranch_execz .LBB0_649

.LBB0_666:
	s_nop 0
	v_exp_f32_e32 v80, v98
	v_exp_f32_e32 v81, v99
	v_exp_f32_e32 v82, v100
	v_exp_f32_e32 v83, v101
	v_exp_f32_e32 v84, v102
	v_exp_f32_e32 v85, v103
	v_exp_f32_e32 v86, v104
	v_exp_f32_e32 v87, v105
	v_exp_f32_e32 v88, v106
	v_exp_f32_e32 v89, v107
	v_exp_f32_e32 v90, v108
	v_exp_f32_e32 v91, v109
	v_exp_f32_e32 v92, v110
	v_exp_f32_e32 v93, v111
	v_exp_f32_e32 v94, v112
	s_cbranch_execz .LBB0_670
.LBB0_671:
	v_exp_f32_e32 v79, v97
	v_exp_f32_e32 v95, v113
	v_cvt_pk_bf16_f32 v96, v64, v65
	v_cvt_pk_bf16_f32 v97, v66, v67
	v_cvt_pk_bf16_f32 v98, v68, v69
	v_cvt_pk_bf16_f32 v99, v70, v71
	v_cvt_pk_bf16_f32 v100, v72, v73
	v_cvt_pk_bf16_f32 v101, v74, v75
	v_cvt_pk_bf16_f32 v102, v76, v77
	v_cvt_pk_bf16_f32 v103, v78, v79
	v_cvt_pk_bf16_f32 v104, v80, v81
	v_cvt_pk_bf16_f32 v105, v82, v83
	v_cvt_pk_bf16_f32 v106, v84, v85
	v_cvt_pk_bf16_f32 v107, v86, v87
	v_cvt_pk_bf16_f32 v108, v88, v89
	v_cvt_pk_bf16_f32 v109, v90, v91
	v_cvt_pk_bf16_f32 v110, v92, v93
	v_cvt_pk_bf16_f32 v111, v94, v95
	v_permlane32_swap_b32_e32 v96, v98
	v_permlane32_swap_b32_e32 v97, v99
	v_permlane32_swap_b32_e32 v100, v102
	v_permlane32_swap_b32_e32 v101, v103
	v_permlane32_swap_b32_e32 v104, v106
	v_permlane32_swap_b32_e32 v105, v107
	v_permlane32_swap_b32_e32 v108, v110
	v_permlane32_swap_b32_e32 v109, v111
	s_waitcnt vmcnt(0)
	v_cndmask_b32_e64 v112, 0, 1, s[48:49]
	v_cmp_ne_u32_e64 s[44:45], 1, v112
	s_andn2_b64 vcc, exec, s[48:49]
	s_waitcnt vmcnt(3)
	ds_write_b128 v232, v[194:197] offset:49152
	s_waitcnt vmcnt(1)
	ds_write_b128 v233, v[202:205] offset:49152
	ds_write_b128 v234, v[198:201] offset:16384
	s_waitcnt vmcnt(0)
	ds_write_b128 v235, v[206:209] offset:16384
	s_waitcnt lgkmcnt(0)
	s_barrier
	s_cbranch_vccnz .LBB0_673
	global_load_dwordx4 v[194:197], v[214:215], off
	global_load_dwordx4 v[202:205], v[216:217], off
	global_load_dwordx4 v[198:201], v[218:219], off
	global_load_dwordx4 v[206:209], v[220:221], off

.LBB0_676:
	s_nop 2
	v_exp_f32_e32 v144, v128
	v_exp_f32_e32 v145, v129
	v_exp_f32_e32 v146, v130
	v_exp_f32_e32 v147, v131
	v_exp_f32_e32 v148, v132
	v_exp_f32_e32 v149, v133
	v_exp_f32_e32 v150, v134
	v_exp_f32_e32 v151, v135
	v_exp_f32_e32 v152, v136
	v_exp_f32_e32 v153, v137
	v_exp_f32_e32 v154, v138
	v_exp_f32_e32 v155, v139
	v_exp_f32_e32 v156, v140
	v_exp_f32_e32 v157, v141
	v_exp_f32_e32 v158, v142
	s_cbranch_execz .LBB0_680
.LBB0_681:
	v_exp_f32_e32 v111, v127
	v_exp_f32_e32 v159, v143
	v_cvt_pk_bf16_f32 v124, v96, v97
	v_cvt_pk_bf16_f32 v125, v98, v99
	v_cvt_pk_bf16_f32 v126, v100, v101
	v_cvt_pk_bf16_f32 v127, v102, v103
	v_cvt_pk_bf16_f32 v120, v104, v105
	v_cvt_pk_bf16_f32 v121, v106, v107
	v_cvt_pk_bf16_f32 v122, v108, v109
	v_cvt_pk_bf16_f32 v123, v110, v111
	v_cvt_pk_bf16_f32 v116, v144, v145
	v_cvt_pk_bf16_f32 v117, v146, v147
	v_cvt_pk_bf16_f32 v118, v148, v149
	v_cvt_pk_bf16_f32 v119, v150, v151
	v_cvt_pk_bf16_f32 v112, v152, v153
	v_cvt_pk_bf16_f32 v113, v154, v155
	v_cvt_pk_bf16_f32 v114, v156, v157
	v_cvt_pk_bf16_f32 v115, v158, v159
	v_permlane32_swap_b32_e32 v124, v126
	v_permlane32_swap_b32_e32 v125, v127
	v_permlane32_swap_b32_e32 v120, v122
	v_permlane32_swap_b32_e32 v121, v123
	v_permlane32_swap_b32_e32 v116, v118
	v_permlane32_swap_b32_e32 v117, v119
	v_permlane32_swap_b32_e32 v112, v114
	v_permlane32_swap_b32_e32 v113, v115
	s_and_b64 vcc, exec, s[44:45]
	s_cbranch_vccnz .LBB0_660
	s_waitcnt vmcnt(0)
	s_waitcnt vmcnt(3)
	ds_write_b128 v232, v[194:197] offset:32768
	s_waitcnt vmcnt(2)
	ds_write_b128 v233, v[202:205] offset:32768
	s_waitcnt vmcnt(1)
	ds_write_b128 v234, v[198:201]
	s_waitcnt vmcnt(0)
	ds_write_b128 v235, v[206:209]
	s_branch .LBB0_660

.LBB0_690:
	s_nop 1
	v_exp_f32_e32 v80, v96
	v_exp_f32_e32 v81, v97
	v_exp_f32_e32 v82, v98
	v_exp_f32_e32 v83, v99
	v_exp_f32_e32 v84, v100
	v_exp_f32_e32 v85, v101
	v_exp_f32_e32 v86, v102
	v_exp_f32_e32 v87, v103
	v_exp_f32_e32 v88, v104
	v_exp_f32_e32 v89, v105
	v_exp_f32_e32 v90, v106
	v_exp_f32_e32 v91, v107
	v_exp_f32_e32 v92, v108
	v_exp_f32_e32 v93, v109
	v_exp_f32_e32 v94, v110
	s_cbranch_execz .LBB0_694
.LBB0_695:
	v_exp_f32_e32 v79, v127
	v_exp_f32_e32 v95, v111
	v_cvt_pk_bf16_f32 v96, v64, v65
	v_cvt_pk_bf16_f32 v97, v66, v67
	v_cvt_pk_bf16_f32 v98, v68, v69
	v_cvt_pk_bf16_f32 v99, v70, v71
	v_cvt_pk_bf16_f32 v100, v72, v73
	v_cvt_pk_bf16_f32 v101, v74, v75
	v_cvt_pk_bf16_f32 v102, v76, v77
	v_cvt_pk_bf16_f32 v103, v78, v79
	v_cvt_pk_bf16_f32 v104, v80, v81
	v_cvt_pk_bf16_f32 v105, v82, v83
	v_cvt_pk_bf16_f32 v106, v84, v85
	v_cvt_pk_bf16_f32 v107, v86, v87
	v_cvt_pk_bf16_f32 v108, v88, v89
	v_cvt_pk_bf16_f32 v109, v90, v91
	v_cvt_pk_bf16_f32 v110, v92, v93
	v_cvt_pk_bf16_f32 v111, v94, v95
	v_permlane32_swap_b32_e32 v96, v98
	v_permlane32_swap_b32_e32 v97, v99
	v_permlane32_swap_b32_e32 v100, v102
	v_permlane32_swap_b32_e32 v101, v103
	v_permlane32_swap_b32_e32 v104, v106
	v_permlane32_swap_b32_e32 v105, v107
	v_permlane32_swap_b32_e32 v108, v110
	v_permlane32_swap_b32_e32 v109, v111
	s_barrier
	ds_read_b64_tr_b16 v[112:113], v231 offset:0
	ds_read_b64_tr_b16 v[114:115], v231 offset:0x800
	ds_read_b64_tr_b16 v[116:117], v231 offset:0x1000
	ds_read_b64_tr_b16 v[118:119], v231 offset:0x1800
	ds_read_b64_tr_b16 v[120:121], v231 offset:0x2000
	ds_read_b64_tr_b16 v[122:123], v231 offset:0x2800
	ds_read_b64_tr_b16 v[124:125], v231 offset:0x3000
	ds_read_b64_tr_b16 v[126:127], v231 offset:0x3800
	s_waitcnt lgkmcnt(0)
	s_nop 0
	v_mfma_f32_32x32x16_bf16 v[0:15], v[96:99], v[112:115], v[0:15]
	ds_read_b64_tr_b16 v[112:113], v231 offset:0x200
	ds_read_b64_tr_b16 v[114:115], v231 offset:0xa00
	v_mfma_f32_32x32x16_bf16 v[0:15], v[100:103], v[116:119], v[0:15]
	ds_read_b64_tr_b16 v[116:117], v231 offset:0x1200
	ds_read_b64_tr_b16 v[118:119], v231 offset:0x1a00
	v_mfma_f32_32x32x16_bf16 v[0:15], v[104:107], v[120:123], v[0:15]
	ds_read_b64_tr_b16 v[120:121], v231 offset:0x2200
	ds_read_b64_tr_b16 v[122:123], v231 offset:0x2a00
	v_mfma_f32_32x32x16_bf16 v[0:15], v[108:111], v[124:127], v[0:15]
	ds_read_b64_tr_b16 v[124:125], v231 offset:0x3200
	ds_read_b64_tr_b16 v[126:127], v231 offset:0x3a00
	s_waitcnt lgkmcnt(0)
	v_mfma_f32_32x32x16_bf16 v[16:31], v[96:99], v[112:115], v[16:31]
	ds_read_b64_tr_b16 v[112:113], v231 offset:0x400
	ds_read_b64_tr_b16 v[114:115], v231 offset:0xc00
	v_mfma_f32_32x32x16_bf16 v[16:31], v[100:103], v[116:119], v[16:31]
	ds_read_b64_tr_b16 v[116:117], v231 offset:0x1400
	ds_read_b64_tr_b16 v[118:119], v231 offset:0x1c00
	v_mfma_f32_32x32x16_bf16 v[16:31], v[104:107], v[120:123], v[16:31]
	ds_read_b64_tr_b16 v[120:121], v231 offset:0x2400
	ds_read_b64_tr_b16 v[122:123], v231 offset:0x2c00
	v_mfma_f32_32x32x16_bf16 v[16:31], v[108:111], v[124:127], v[16:31]
	ds_read_b64_tr_b16 v[124:125], v231 offset:0x3400
	ds_read_b64_tr_b16 v[126:127], v231 offset:0x3c00
	s_waitcnt lgkmcnt(0)
	v_mfma_f32_32x32x16_bf16 v[32:47], v[96:99], v[112:115], v[32:47]
	ds_read_b64_tr_b16 v[112:113], v231 offset:0x600
	ds_read_b64_tr_b16 v[114:115], v231 offset:0xe00
	v_mfma_f32_32x32x16_bf16 v[32:47], v[100:103], v[116:119], v[32:47]
	ds_read_b64_tr_b16 v[116:117], v231 offset:0x1600
	ds_read_b64_tr_b16 v[118:119], v231 offset:0x1e00
	v_mfma_f32_32x32x16_bf16 v[32:47], v[104:107], v[120:123], v[32:47]
	ds_read_b64_tr_b16 v[120:121], v231 offset:0x2600
	ds_read_b64_tr_b16 v[122:123], v231 offset:0x2e00
	v_mfma_f32_32x32x16_bf16 v[32:47], v[108:111], v[124:127], v[32:47]
	ds_read_b64_tr_b16 v[124:125], v231 offset:0x3600
	ds_read_b64_tr_b16 v[126:127], v231 offset:0x3e00
	s_waitcnt lgkmcnt(0)
	v_mfma_f32_32x32x16_bf16 v[48:63], v[96:99], v[112:115], v[48:63]
	s_waitcnt vmcnt(0)
	v_cndmask_b32_e64 v96, 0, 1, s[48:49]
	v_cmp_ne_u32_e64 s[44:45], 1, v96
	s_andn2_b64 vcc, exec, s[48:49]
	s_waitcnt vmcnt(3)
	ds_write_b128 v232, v[146:149] offset:49152
	s_waitcnt vmcnt(1)
	ds_write_b128 v233, v[154:157] offset:49152
	ds_write_b128 v234, v[150:153] offset:16384
	s_waitcnt vmcnt(0)
	ds_write_b128 v235, v[194:197] offset:16384
	s_waitcnt lgkmcnt(0)
	v_mfma_f32_32x32x16_bf16 v[48:63], v[100:103], v[116:119], v[48:63]
	s_barrier
	v_mfma_f32_32x32x16_bf16 v[48:63], v[104:107], v[120:123], v[48:63]
	v_mfma_f32_32x32x16_bf16 v[48:63], v[108:111], v[124:127], v[48:63]
	s_cbranch_vccnz .LBB0_697
	global_load_dwordx4 v[146:149], v[158:159], off
	global_load_dwordx4 v[154:157], v[198:199], off
	global_load_dwordx4 v[150:153], v[200:201], off
	global_load_dwordx4 v[194:197], v[202:203], off

.LBB0_700:
	s_nop 3
	v_exp_f32_e32 v112, v130
	v_exp_f32_e32 v113, v131
	v_exp_f32_e32 v114, v132
	v_exp_f32_e32 v115, v133
	v_exp_f32_e32 v116, v134
	v_exp_f32_e32 v117, v135
	v_exp_f32_e32 v118, v136
	v_exp_f32_e32 v119, v137
	v_exp_f32_e32 v120, v138
	v_exp_f32_e32 v121, v139
	v_exp_f32_e32 v122, v140
	v_exp_f32_e32 v123, v141
	v_exp_f32_e32 v124, v142
	v_exp_f32_e32 v125, v143
	v_exp_f32_e32 v126, v144
	s_cbranch_execz .LBB0_704
.LBB0_705:
	v_exp_f32_e32 v111, v129
	s_nop 0
	v_exp_f32_e32 v127, v145
	v_cvt_pk_bf16_f32 v128, v96, v97
	v_cvt_pk_bf16_f32 v129, v98, v99
	v_cvt_pk_bf16_f32 v130, v100, v101
	v_cvt_pk_bf16_f32 v131, v102, v103
	v_cvt_pk_bf16_f32 v132, v104, v105
	v_cvt_pk_bf16_f32 v133, v106, v107
	v_cvt_pk_bf16_f32 v134, v108, v109
	v_cvt_pk_bf16_f32 v135, v110, v111
	v_cvt_pk_bf16_f32 v136, v112, v113
	v_cvt_pk_bf16_f32 v137, v114, v115
	v_cvt_pk_bf16_f32 v138, v116, v117
	v_cvt_pk_bf16_f32 v139, v118, v119
	v_cvt_pk_bf16_f32 v140, v120, v121
	v_cvt_pk_bf16_f32 v141, v122, v123
	v_cvt_pk_bf16_f32 v142, v124, v125
	v_cvt_pk_bf16_f32 v143, v126, v127
	v_permlane32_swap_b32_e32 v128, v130
	v_permlane32_swap_b32_e32 v129, v131
	v_permlane32_swap_b32_e32 v132, v134
	v_permlane32_swap_b32_e32 v133, v135
	v_permlane32_swap_b32_e32 v136, v138
	v_permlane32_swap_b32_e32 v137, v139
	v_permlane32_swap_b32_e32 v140, v142
	v_permlane32_swap_b32_e32 v141, v143
	s_barrier
	ds_read_b64_tr_b16 v[216:217], v160 offset:0
	ds_read_b64_tr_b16 v[218:219], v160 offset:0x800
	ds_read_b64_tr_b16 v[226:227], v160 offset:0x1000
	ds_read_b64_tr_b16 v[228:229], v160 offset:0x1800
	ds_read_b64_tr_b16 v[236:237], v160 offset:0x2000
	ds_read_b64_tr_b16 v[238:239], v160 offset:0x2800
	ds_read_b64_tr_b16 v[246:247], v160 offset:0x3000
	ds_read_b64_tr_b16 v[248:249], v160 offset:0x3800
	s_waitcnt lgkmcnt(0)
	s_nop 0
	v_mfma_f32_32x32x16_bf16 v[0:15], v[128:131], v[216:219], v[0:15]
	ds_read_b64_tr_b16 v[216:217], v160 offset:0x200
	ds_read_b64_tr_b16 v[218:219], v160 offset:0xa00
	v_mfma_f32_32x32x16_bf16 v[0:15], v[132:135], v[226:229], v[0:15]
	ds_read_b64_tr_b16 v[226:227], v160 offset:0x1200
	ds_read_b64_tr_b16 v[228:229], v160 offset:0x1a00
	v_mfma_f32_32x32x16_bf16 v[0:15], v[136:139], v[236:239], v[0:15]
	ds_read_b64_tr_b16 v[236:237], v160 offset:0x2200
	ds_read_b64_tr_b16 v[238:239], v160 offset:0x2a00
	v_mfma_f32_32x32x16_bf16 v[0:15], v[140:143], v[246:249], v[0:15]
	ds_read_b64_tr_b16 v[246:247], v160 offset:0x3200
	ds_read_b64_tr_b16 v[248:249], v160 offset:0x3a00
	s_waitcnt lgkmcnt(0)
	v_mfma_f32_32x32x16_bf16 v[16:31], v[128:131], v[216:219], v[16:31]
	ds_read_b64_tr_b16 v[216:217], v160 offset:0x400
	ds_read_b64_tr_b16 v[218:219], v160 offset:0xc00
	v_mfma_f32_32x32x16_bf16 v[16:31], v[132:135], v[226:229], v[16:31]
	ds_read_b64_tr_b16 v[226:227], v160 offset:0x1400
	ds_read_b64_tr_b16 v[228:229], v160 offset:0x1c00
	v_mfma_f32_32x32x16_bf16 v[16:31], v[136:139], v[236:239], v[16:31]
	ds_read_b64_tr_b16 v[236:237], v160 offset:0x2400
	ds_read_b64_tr_b16 v[238:239], v160 offset:0x2c00
	v_mfma_f32_32x32x16_bf16 v[16:31], v[140:143], v[246:249], v[16:31]
	ds_read_b64_tr_b16 v[246:247], v160 offset:0x3400
	ds_read_b64_tr_b16 v[248:249], v160 offset:0x3c00
	s_waitcnt lgkmcnt(0)
	v_mfma_f32_32x32x16_bf16 v[32:47], v[128:131], v[216:219], v[32:47]
	ds_read_b64_tr_b16 v[216:217], v160 offset:0x600
	ds_read_b64_tr_b16 v[218:219], v160 offset:0xe00
	v_mfma_f32_32x32x16_bf16 v[32:47], v[132:135], v[226:229], v[32:47]
	ds_read_b64_tr_b16 v[226:227], v160 offset:0x1600
	ds_read_b64_tr_b16 v[228:229], v160 offset:0x1e00
	v_mfma_f32_32x32x16_bf16 v[32:47], v[136:139], v[236:239], v[32:47]
	ds_read_b64_tr_b16 v[236:237], v160 offset:0x2600
	ds_read_b64_tr_b16 v[238:239], v160 offset:0x2e00
	v_mfma_f32_32x32x16_bf16 v[32:47], v[140:143], v[246:249], v[32:47]
	ds_read_b64_tr_b16 v[246:247], v160 offset:0x3600
	ds_read_b64_tr_b16 v[248:249], v160 offset:0x3e00
	s_waitcnt lgkmcnt(0)
	v_mfma_f32_32x32x16_bf16 v[48:63], v[128:131], v[216:219], v[48:63]
	s_and_b64 vcc, exec, s[44:45]
	v_mfma_f32_32x32x16_bf16 v[48:63], v[132:135], v[226:229], v[48:63]
	v_mfma_f32_32x32x16_bf16 v[48:63], v[136:139], v[236:239], v[48:63]
	v_mfma_f32_32x32x16_bf16 v[48:63], v[140:143], v[246:249], v[48:63]
	s_cbranch_vccnz .LBB0_686
	s_waitcnt vmcnt(0)
	s_waitcnt vmcnt(3)
	ds_write_b128 v232, v[146:149] offset:32768
	s_waitcnt vmcnt(2)
	ds_write_b128 v233, v[154:157] offset:32768
	s_waitcnt vmcnt(1)
	ds_write_b128 v234, v[150:153]
	s_waitcnt vmcnt(0)
	ds_write_b128 v235, v[194:197]
	s_branch .LBB0_686
